# speedup vs baseline: 1.0027x; 1.0027x over previous
.LBB1_241:
	v_mov_b64_e32 v[86:87], v[80:81]
	s_mov_b32 s0, 0x80000
	s_mov_b32 s1, 0
	v_lshl_add_u64 v[88:89], v[80:81], 0, s[0:1]
	v_cvt_pk_f16_f32 v64, v52, v53
	v_cvt_pk_f16_f32 v65, v54, v55
	v_cvt_pk_f16_f32 v66, v48, v49
	v_cvt_pk_f16_f32 v67, v50, v51
	global_store_dwordx4 v[88:89], v[64:67], off
	v_cvt_pk_f16_f32 v68, v44, v45
	v_cvt_pk_f16_f32 v69, v46, v47
	v_cvt_pk_f16_f32 v70, v40, v41
	v_cvt_pk_f16_f32 v71, v42, v43
	global_store_dwordx4 v[86:87], v[68:71], off offset:1024
	v_cvt_pk_f16_f32 v72, v36, v37
	v_cvt_pk_f16_f32 v73, v38, v39
	v_cvt_pk_f16_f32 v74, v32, v33
	v_cvt_pk_f16_f32 v75, v34, v35
	global_store_dwordx4 v[88:89], v[72:75], off offset:1024
	v_cvt_pk_f16_f32 v76, v28, v29
	v_cvt_pk_f16_f32 v77, v30, v31
	v_cvt_pk_f16_f32 v78, v24, v25
	v_cvt_pk_f16_f32 v79, v26, v27
	global_store_dwordx4 v[86:87], v[76:79], off offset:2048
	v_cvt_pk_f16_f32 v64, v20, v21
	v_cvt_pk_f16_f32 v65, v22, v23
	v_cvt_pk_f16_f32 v66, v16, v17
	v_cvt_pk_f16_f32 v67, v18, v19
	global_store_dwordx4 v[88:89], v[64:67], off offset:2048
	v_cvt_pk_f16_f32 v68, v12, v13
	v_cvt_pk_f16_f32 v69, v14, v15
	v_cvt_pk_f16_f32 v70, v8, v9
	v_cvt_pk_f16_f32 v71, v10, v11
	global_store_dwordx4 v[86:87], v[68:71], off offset:3072
	v_cvt_pk_f16_f32 v72, v4, v5
	v_cvt_pk_f16_f32 v73, v6, v7
	v_cvt_pk_f16_f32 v74, v0, v1
	v_cvt_pk_f16_f32 v75, v2, v3
	global_store_dwordx4 v[88:89], v[72:75], off offset:3072
	s_branch .LBB1_217
